# conversion batching now guarded: falls back to the one-chunk-per-iteration code unless the prep runs on exactly 1024 waves
# baseline (speedup 1.0000x reference)
; __device__ __forceinline__ void cvt8_chunk(const float* src, unsigned char* dst, size_t chunk, int lane, float sc) {
;     const f32x4* s = (const f32x4*)(src + chunk * 512) + lane * 2; const f32x4 a = s[0] * sc, b = s[1] * sc;
;     int w0 = 0, w1 = 0;
;     w0 = __builtin_amdgcn_cvt_pk_fp8_f32(a.x, a.y, w0, false); w0 = __builtin_amdgcn_cvt_pk_fp8_f32(a.z, a.w, w0, true);
;     w1 = __builtin_amdgcn_cvt_pk_fp8_f32(b.x, b.y, w1, false); w1 = __builtin_amdgcn_cvt_pk_fp8_f32(b.z, b.w, w1, true);
;     *(v2u*)(dst + chunk * 512 + lane * 8) = (v2u){(unsigned)w0, (unsigned)w1};
; }
; __device__ __forceinline__ void prep_phase(Frame& F, const Args& a, int layer, int blk, int nblk_, int part) {
;     ...
;         for (int it = gw; it < ntot; it += NGW) {
;             int r = it;
;             if (r < n2) { cvt8_chunk(ut, (unsigned char*)(db + DB_U), r, lane, 256.f); continue; } r -= n2;
;             if (r < n2) { cvt8_chunk(vt, (unsigned char*)(db + DB_V), r, lane, 64.f); continue; } r -= n2;
.LBB0_1194:
	v_readlane_b32 vcc_lo, v254, 44
	s_cmp_lg_u32 vcc_lo, 0x400
	s_cbranch_scc1 .Lcv_2_orig
	v_lshl_add_u64 v[6:7], v[2:3], 4, s[36:37]
	s_lshl_b64 s[36:37], s[22:23], 9
	s_lshl_b64 s[22:23], s[22:23], 11
	v_lshl_add_u64 v[150:151], v[6:7], 0, s[22:23]
	v_lshl_add_u64 v[14:15], v[4:5], 0, s[38:39]
	global_load_dwordx4 v[104:107], v[150:151], off offset:16
	global_load_dwordx4 v[100:103], v[150:151], off
	v_add_co_u32_e32 v150, vcc, 0x200000, v150
	s_nop 1
	v_addc_co_u32_e32 v151, vcc, 0, v151, vcc
	global_load_dwordx4 v[112:115], v[150:151], off offset:16
	global_load_dwordx4 v[108:111], v[150:151], off
	v_add_co_u32_e32 v150, vcc, 0x200000, v150
	s_nop 1
	v_addc_co_u32_e32 v151, vcc, 0, v151, vcc
	global_load_dwordx4 v[120:123], v[150:151], off offset:16
	global_load_dwordx4 v[116:119], v[150:151], off
	v_add_co_u32_e32 v150, vcc, 0x200000, v150
	s_nop 1
	v_addc_co_u32_e32 v151, vcc, 0, v151, vcc
	global_load_dwordx4 v[128:131], v[150:151], off offset:16
	global_load_dwordx4 v[124:127], v[150:151], off
	v_lshl_add_u64 v[148:149], v[14:15], 0, s[36:37]
	s_waitcnt vmcnt(6)
	v_mov_b32_e32 v132, v0
	v_mov_b32_e32 v133, v0
	v_pk_mul_f32 v[104:105], v[104:105], s[20:21] op_sel_hi:[1,0]
	v_pk_mul_f32 v[100:101], v[100:101], s[20:21] op_sel_hi:[1,0]
	v_cvt_pk_fp8_f32 v133, v104, v105
	v_cvt_pk_fp8_f32 v132, v100, v101
	v_pk_mul_f32 v[102:103], v[102:103], s[20:21] op_sel_hi:[1,0]
	v_pk_mul_f32 v[106:107], v[106:107], s[20:21] op_sel_hi:[1,0]
	v_cvt_pk_fp8_f32 v132, v102, v103 op_sel:[0,0,1]
	v_cvt_pk_fp8_f32 v133, v106, v107 op_sel:[0,0,1]
	global_store_dwordx2 v[148:149], v[132:133], off
	s_waitcnt vmcnt(5)
	v_mov_b32_e32 v134, v0
	v_mov_b32_e32 v135, v0
	v_pk_mul_f32 v[112:113], v[112:113], s[20:21] op_sel_hi:[1,0]
	v_pk_mul_f32 v[108:109], v[108:109], s[20:21] op_sel_hi:[1,0]
	v_cvt_pk_fp8_f32 v135, v112, v113
	v_cvt_pk_fp8_f32 v134, v108, v109
	v_pk_mul_f32 v[110:111], v[110:111], s[20:21] op_sel_hi:[1,0]
	v_pk_mul_f32 v[114:115], v[114:115], s[20:21] op_sel_hi:[1,0]
	v_cvt_pk_fp8_f32 v134, v110, v111 op_sel:[0,0,1]
	v_cvt_pk_fp8_f32 v135, v114, v115 op_sel:[0,0,1]
	v_add_co_u32_e32 v148, vcc, 0x80000, v148
	s_nop 1
	v_addc_co_u32_e32 v149, vcc, 0, v149, vcc
	global_store_dwordx2 v[148:149], v[134:135], off
	s_waitcnt vmcnt(4)
	v_mov_b32_e32 v136, v0
	v_mov_b32_e32 v137, v0
	v_pk_mul_f32 v[120:121], v[120:121], s[20:21] op_sel_hi:[1,0]
	v_pk_mul_f32 v[116:117], v[116:117], s[20:21] op_sel_hi:[1,0]
	v_cvt_pk_fp8_f32 v137, v120, v121
	v_cvt_pk_fp8_f32 v136, v116, v117
	v_pk_mul_f32 v[118:119], v[118:119], s[20:21] op_sel_hi:[1,0]
	v_pk_mul_f32 v[122:123], v[122:123], s[20:21] op_sel_hi:[1,0]
	v_cvt_pk_fp8_f32 v136, v118, v119 op_sel:[0,0,1]
	v_cvt_pk_fp8_f32 v137, v122, v123 op_sel:[0,0,1]
	v_add_co_u32_e32 v148, vcc, 0x80000, v148
	s_nop 1
	v_addc_co_u32_e32 v149, vcc, 0, v149, vcc
	global_store_dwordx2 v[148:149], v[136:137], off
	s_waitcnt vmcnt(3)
	v_mov_b32_e32 v138, v0
	v_mov_b32_e32 v139, v0
	v_pk_mul_f32 v[128:129], v[128:129], s[20:21] op_sel_hi:[1,0]
	v_pk_mul_f32 v[124:125], v[124:125], s[20:21] op_sel_hi:[1,0]
	v_cvt_pk_fp8_f32 v139, v128, v129
	v_cvt_pk_fp8_f32 v138, v124, v125
	v_pk_mul_f32 v[126:127], v[126:127], s[20:21] op_sel_hi:[1,0]
	v_pk_mul_f32 v[130:131], v[130:131], s[20:21] op_sel_hi:[1,0]
	v_cvt_pk_fp8_f32 v138, v126, v127 op_sel:[0,0,1]
	v_cvt_pk_fp8_f32 v139, v130, v131 op_sel:[0,0,1]
	v_add_co_u32_e32 v148, vcc, 0x80000, v148
	s_nop 1
	v_addc_co_u32_e32 v149, vcc, 0, v149, vcc
	global_store_dwordx2 v[148:149], v[138:139], off
	v_readlane_b32 s20, v254, 44
	v_readlane_b32 s21, v254, 45
	s_lshl_b64 s[20:21], s[20:21], 2
	s_add_u32 s2, s2, s20
	s_addc_u32 s3, s3, s21
	s_cmp_lt_i32 s2, 0x10000
	s_cbranch_scc0 .LBB0_1197
	s_branch .LBB0_1195

; __device__ __forceinline__ u32x4 pk8(const f32x4 a, const f32x4 b) { u32x4 w; w.x = cvt_pk_bf16(a[0], a[1]); w.y = cvt_pk_bf16(a[2], a[3]); w.z = cvt_pk_bf16(b[0], b[1]); w.w = cvt_pk_bf16(b[2], b[3]); return w; }
; __device__ __forceinline__ void cvt_chunk(const float* src, bf16* dst, size_t chunk, int lane) {
;     const f32x4* s = (const f32x4*)(src + chunk * 512) + lane * 2; const f32x4 a = s[0], b = s[1];
;     *(v4u*)(dst + chunk * 512 + lane * 8) = pk8(a, b);
; }
; __device__ __forceinline__ void prep_phase(Frame& F, const Args& a, int layer, int blk, int nblk_, int part) {
;     ...
;         for (int it = gw; it < ntot; it += NGW) {
;             int r = it;
;             if (r < n2) { cvt8_chunk(ut, (unsigned char*)(db + DB_U), r, lane, 256.f); continue; } r -= n2;
;             if (r < n2) { cvt8_chunk(vt, (unsigned char*)(db + DB_V), r, lane, 64.f); continue; } r -= n2;
;             if (r < n4) { cvt_chunk(pin, (bf16*)(db + DB_PB), r, lane); continue; } r -= n4;
.LBB0_1300:
	s_andn2_b64 vcc, exec, s[22:23]
	s_cbranch_vccnz .LBB0_1302
	v_readlane_b32 s22, v254, 44
	s_cmp_lg_u32 s22, 0x400
	s_cbranch_scc1 .Lcv_p_orig
	s_add_i32 s22, s5, 0x8000
	s_and_b32 s22, s22, 0xc00
	s_cmp_lg_u32 s22, 0
	s_cbranch_scc1 .LBB0_1302
	v_readlane_b32 s22, v254, 30
	s_add_i32 s22, s22, s36
	s_add_i32 s30, s22, 0xfe000000
	v_lshl_add_u64 v[150:151], s[30:31], 2, v[10:11]
	global_load_dwordx4 v[100:103], v[150:151], off
	global_load_dwordx4 v[104:107], v[150:151], off offset:16
	v_add_co_u32_e32 v150, vcc, 0x200000, v150
	s_nop 1
	v_addc_co_u32_e32 v151, vcc, 0, v151, vcc
	global_load_dwordx4 v[108:111], v[150:151], off
	global_load_dwordx4 v[112:115], v[150:151], off offset:16
	v_add_co_u32_e32 v150, vcc, 0x200000, v150
	s_nop 1
	v_addc_co_u32_e32 v151, vcc, 0, v151, vcc
	global_load_dwordx4 v[116:119], v[150:151], off
	global_load_dwordx4 v[120:123], v[150:151], off offset:16
	v_add_co_u32_e32 v150, vcc, 0x200000, v150
	s_nop 1
	v_addc_co_u32_e32 v151, vcc, 0, v151, vcc
	global_load_dwordx4 v[124:127], v[150:151], off
	global_load_dwordx4 v[128:131], v[150:151], off offset:16
	v_lshl_add_u64 v[148:149], s[30:31], 1, v[12:13]
	s_waitcnt vmcnt(6)
	v_cvt_pk_bf16_f32 v100, v100, v101
	v_cvt_pk_bf16_f32 v101, v102, v103
	v_cvt_pk_bf16_f32 v102, v104, v105
	v_cvt_pk_bf16_f32 v103, v106, v107
	global_store_dwordx4 v[148:149], v[100:103], off
	s_waitcnt vmcnt(5)
	v_cvt_pk_bf16_f32 v108, v108, v109
	v_cvt_pk_bf16_f32 v109, v110, v111
	v_cvt_pk_bf16_f32 v110, v112, v113
	v_cvt_pk_bf16_f32 v111, v114, v115
	v_add_co_u32_e32 v148, vcc, 0x100000, v148
	s_nop 1
	v_addc_co_u32_e32 v149, vcc, 0, v149, vcc
	global_store_dwordx4 v[148:149], v[108:111], off
	s_waitcnt vmcnt(4)
	v_cvt_pk_bf16_f32 v116, v116, v117
	v_cvt_pk_bf16_f32 v117, v118, v119
	v_cvt_pk_bf16_f32 v118, v120, v121
	v_cvt_pk_bf16_f32 v119, v122, v123
	v_add_co_u32_e32 v148, vcc, 0x100000, v148
	s_nop 1
	v_addc_co_u32_e32 v149, vcc, 0, v149, vcc
	global_store_dwordx4 v[148:149], v[116:119], off
	s_waitcnt vmcnt(3)
	v_cvt_pk_bf16_f32 v124, v124, v125
	v_cvt_pk_bf16_f32 v125, v126, v127
	v_cvt_pk_bf16_f32 v126, v128, v129
	v_cvt_pk_bf16_f32 v127, v130, v131
	v_add_co_u32_e32 v148, vcc, 0x100000, v148
	s_nop 1
	v_addc_co_u32_e32 v149, vcc, 0, v149, vcc
	global_store_dwordx4 v[148:149], v[124:127], off
	s_branch .LBB0_1302
.Lcv_p_orig:
	v_readlane_b32 s22, v254, 30
	s_add_i32 s22, s22, s36
	s_add_i32 s30, s22, 0xfe000000
	v_lshl_add_u64 v[30:31], s[30:31], 2, v[10:11]
	global_load_dwordx4 v[26:29], v[30:31], off
	s_nop 0
	global_load_dwordx4 v[30:33], v[30:31], off offset:16
	s_waitcnt vmcnt(0)
	v_cvt_pk_bf16_f32 v26, v26, v27
	v_cvt_pk_bf16_f32 v27, v28, v29
	v_cvt_pk_bf16_f32 v28, v30, v31
	v_lshl_add_u64 v[30:31], s[30:31], 1, v[12:13]
	v_cvt_pk_bf16_f32 v29, v32, v33
	global_store_dwordx4 v[30:31], v[26:29], off

; __device__ __forceinline__ void cvt8_chunk(const float* src, unsigned char* dst, size_t chunk, int lane, float sc) {
;     const f32x4* s = (const f32x4*)(src + chunk * 512) + lane * 2; const f32x4 a = s[0] * sc, b = s[1] * sc;
;     int w0 = 0, w1 = 0;
;     w0 = __builtin_amdgcn_cvt_pk_fp8_f32(a.x, a.y, w0, false); w0 = __builtin_amdgcn_cvt_pk_fp8_f32(a.z, a.w, w0, true);
;     w1 = __builtin_amdgcn_cvt_pk_fp8_f32(b.x, b.y, w1, false); w1 = __builtin_amdgcn_cvt_pk_fp8_f32(b.z, b.w, w1, true);
;     *(v2u*)(dst + chunk * 512 + lane * 8) = (v2u){(unsigned)w0, (unsigned)w1};
; }
; __device__ __forceinline__ void prep_phase(Frame& F, const Args& a, int layer, int blk, int nblk_, int part) {
;     ...
;             if (r < n2) { cvt8_chunk(vt, (unsigned char*)(db + DB_V), r, lane, 64.f); continue; } r -= n2;
.LBB0_1303:
	s_andn2_b64 vcc, exec, s[22:23]
	s_cbranch_vccnz .LBB0_1305
	v_readlane_b32 s22, v254, 44
	s_cmp_lg_u32 s22, 0x400
	s_cbranch_scc1 .Lcv_v_orig
	s_add_i32 s22, s5, 0x8000
	s_and_b32 s22, s22, 0xc00
	s_cmp_lg_u32 s22, 0
	s_cbranch_scc1 .LBB0_1305
	v_readlane_b32 s22, v254, 30
	s_add_i32 s22, s22, s36
	s_add_i32 s30, s22, 0xff000000
	v_lshl_add_u64 v[150:151], s[30:31], 2, v[14:15]
	s_mov_b32 s22, 0x42800000
	global_load_dwordx4 v[104:107], v[150:151], off offset:16
	global_load_dwordx4 v[100:103], v[150:151], off
	v_add_co_u32_e32 v150, vcc, 0x200000, v150
	s_nop 1
	v_addc_co_u32_e32 v151, vcc, 0, v151, vcc
	global_load_dwordx4 v[112:115], v[150:151], off offset:16
	global_load_dwordx4 v[108:111], v[150:151], off
	v_add_co_u32_e32 v150, vcc, 0x200000, v150
	s_nop 1
	v_addc_co_u32_e32 v151, vcc, 0, v151, vcc
	global_load_dwordx4 v[120:123], v[150:151], off offset:16
	global_load_dwordx4 v[116:119], v[150:151], off
	v_add_co_u32_e32 v150, vcc, 0x200000, v150
	s_nop 1
	v_addc_co_u32_e32 v151, vcc, 0, v151, vcc
	global_load_dwordx4 v[128:131], v[150:151], off offset:16
	global_load_dwordx4 v[124:127], v[150:151], off
	v_lshl_add_u64 v[148:149], v[16:17], 0, s[30:31]
	s_waitcnt vmcnt(6)
	v_mov_b32_e32 v132, v0
	v_mov_b32_e32 v133, v0
	v_pk_mul_f32 v[104:105], v[104:105], s[22:23] op_sel_hi:[1,0]
	v_pk_mul_f32 v[100:101], v[100:101], s[22:23] op_sel_hi:[1,0]
	v_cvt_pk_fp8_f32 v133, v104, v105
	v_cvt_pk_fp8_f32 v132, v100, v101
	v_pk_mul_f32 v[102:103], v[102:103], s[22:23] op_sel_hi:[1,0]
	v_pk_mul_f32 v[106:107], v[106:107], s[22:23] op_sel_hi:[1,0]
	v_cvt_pk_fp8_f32 v132, v102, v103 op_sel:[0,0,1]
	v_cvt_pk_fp8_f32 v133, v106, v107 op_sel:[0,0,1]
	global_store_dwordx2 v[148:149], v[132:133], off
	s_waitcnt vmcnt(5)
	v_mov_b32_e32 v134, v0
	v_mov_b32_e32 v135, v0
	v_pk_mul_f32 v[112:113], v[112:113], s[22:23] op_sel_hi:[1,0]
	v_pk_mul_f32 v[108:109], v[108:109], s[22:23] op_sel_hi:[1,0]
	v_cvt_pk_fp8_f32 v135, v112, v113
	v_cvt_pk_fp8_f32 v134, v108, v109
	v_pk_mul_f32 v[110:111], v[110:111], s[22:23] op_sel_hi:[1,0]
	v_pk_mul_f32 v[114:115], v[114:115], s[22:23] op_sel_hi:[1,0]
	v_cvt_pk_fp8_f32 v134, v110, v111 op_sel:[0,0,1]
	v_cvt_pk_fp8_f32 v135, v114, v115 op_sel:[0,0,1]
	v_add_co_u32_e32 v148, vcc, 0x80000, v148
	s_nop 1
	v_addc_co_u32_e32 v149, vcc, 0, v149, vcc
	global_store_dwordx2 v[148:149], v[134:135], off
	s_waitcnt vmcnt(4)
	v_mov_b32_e32 v136, v0
	v_mov_b32_e32 v137, v0
	v_pk_mul_f32 v[120:121], v[120:121], s[22:23] op_sel_hi:[1,0]
	v_pk_mul_f32 v[116:117], v[116:117], s[22:23] op_sel_hi:[1,0]
	v_cvt_pk_fp8_f32 v137, v120, v121
	v_cvt_pk_fp8_f32 v136, v116, v117
	v_pk_mul_f32 v[118:119], v[118:119], s[22:23] op_sel_hi:[1,0]
	v_pk_mul_f32 v[122:123], v[122:123], s[22:23] op_sel_hi:[1,0]
	v_cvt_pk_fp8_f32 v136, v118, v119 op_sel:[0,0,1]
	v_cvt_pk_fp8_f32 v137, v122, v123 op_sel:[0,0,1]
	v_add_co_u32_e32 v148, vcc, 0x80000, v148
	s_nop 1
	v_addc_co_u32_e32 v149, vcc, 0, v149, vcc
	global_store_dwordx2 v[148:149], v[136:137], off
	s_waitcnt vmcnt(3)
	v_mov_b32_e32 v138, v0
	v_mov_b32_e32 v139, v0
	v_pk_mul_f32 v[128:129], v[128:129], s[22:23] op_sel_hi:[1,0]
	v_pk_mul_f32 v[124:125], v[124:125], s[22:23] op_sel_hi:[1,0]
	v_cvt_pk_fp8_f32 v139, v128, v129
	v_cvt_pk_fp8_f32 v138, v124, v125
	v_pk_mul_f32 v[126:127], v[126:127], s[22:23] op_sel_hi:[1,0]
	v_pk_mul_f32 v[130:131], v[130:131], s[22:23] op_sel_hi:[1,0]
	v_cvt_pk_fp8_f32 v138, v126, v127 op_sel:[0,0,1]
	v_cvt_pk_fp8_f32 v139, v130, v131 op_sel:[0,0,1]
	v_add_co_u32_e32 v148, vcc, 0x80000, v148
	s_nop 1
	v_addc_co_u32_e32 v149, vcc, 0, v149, vcc
	global_store_dwordx2 v[148:149], v[138:139], off
	s_branch .LBB0_1305
.Lcv_v_orig:
	v_readlane_b32 s22, v254, 30
	s_add_i32 s22, s22, s36
	s_add_i32 s30, s22, 0xff000000
	v_lshl_add_u64 v[30:31], s[30:31], 2, v[14:15]
	global_load_dwordx4 v[26:29], v[30:31], off offset:16
	s_nop 0
	global_load_dwordx4 v[30:33], v[30:31], off
	s_mov_b32 s22, 0x42800000
	v_mov_b32_e32 v34, v0
	v_mov_b32_e32 v35, v0
	s_waitcnt vmcnt(0)
	v_pk_mul_f32 v[26:27], v[26:27], s[22:23] op_sel_hi:[1,0]
	v_pk_mul_f32 v[30:31], v[30:31], s[22:23] op_sel_hi:[1,0]
	v_cvt_pk_fp8_f32 v35, v26, v27
	v_cvt_pk_fp8_f32 v34, v30, v31
	v_pk_mul_f32 v[32:33], v[32:33], s[22:23] op_sel_hi:[1,0]
	v_pk_mul_f32 v[28:29], v[28:29], s[22:23] op_sel_hi:[1,0]
	v_lshl_add_u64 v[26:27], v[16:17], 0, s[30:31]
	v_cvt_pk_fp8_f32 v34, v32, v33 op_sel:[0,0,1]
	v_cvt_pk_fp8_f32 v35, v28, v29 op_sel:[0,0,1]
	global_store_dwordx2 v[26:27], v[34:35], off

; __device__ __forceinline__ void cvt8_chunk(const float* src, unsigned char* dst, size_t chunk, int lane, float sc) {
;     const f32x4* s = (const f32x4*)(src + chunk * 512) + lane * 2; const f32x4 a = s[0] * sc, b = s[1] * sc;
;     int w0 = 0, w1 = 0;
;     w0 = __builtin_amdgcn_cvt_pk_fp8_f32(a.x, a.y, w0, false); w0 = __builtin_amdgcn_cvt_pk_fp8_f32(a.z, a.w, w0, true);
;     w1 = __builtin_amdgcn_cvt_pk_fp8_f32(b.x, b.y, w1, false); w1 = __builtin_amdgcn_cvt_pk_fp8_f32(b.z, b.w, w1, true);
;     *(v2u*)(dst + chunk * 512 + lane * 8) = (v2u){(unsigned)w0, (unsigned)w1};
; }
; __device__ __forceinline__ void prep_phase(Frame& F, const Args& a, int layer, int blk, int nblk_, int part) {
;     ...
;             if (r < n2) { cvt8_chunk(ut, (unsigned char*)(db + DB_U), r, lane, 256.f); continue; } r -= n2;
.LBB0_1306:
	s_andn2_b64 vcc, exec, s[22:23]
	s_cbranch_vccnz .LBB0_1291
	v_readlane_b32 s22, v254, 44
	s_cmp_lg_u32 s22, 0x400
	s_cbranch_scc1 .Lcv_u_orig
	s_add_i32 s22, s5, 0x8000
	s_and_b32 s22, s22, 0xc00
	s_cmp_lg_u32 s22, 0
	s_cbranch_scc1 .LBB0_1291
	v_lshl_add_u64 v[150:151], s[20:21], 0, v[4:5]
	global_load_dwordx4 v[104:107], v[150:151], off offset:16
	global_load_dwordx4 v[100:103], v[150:151], off
	v_add_co_u32_e32 v150, vcc, 0x200000, v150
	s_nop 1
	v_addc_co_u32_e32 v151, vcc, 0, v151, vcc
	global_load_dwordx4 v[112:115], v[150:151], off offset:16
	global_load_dwordx4 v[108:111], v[150:151], off
	v_add_co_u32_e32 v150, vcc, 0x200000, v150
	s_nop 1
	v_addc_co_u32_e32 v151, vcc, 0, v151, vcc
	global_load_dwordx4 v[120:123], v[150:151], off offset:16
	global_load_dwordx4 v[116:119], v[150:151], off
	v_add_co_u32_e32 v150, vcc, 0x200000, v150
	s_nop 1
	v_addc_co_u32_e32 v151, vcc, 0, v151, vcc
	global_load_dwordx4 v[128:131], v[150:151], off offset:16
	global_load_dwordx4 v[124:127], v[150:151], off
	v_mov_b64_e32 v[148:149], v[2:3]
	s_waitcnt vmcnt(6)
	v_mov_b32_e32 v132, v0
	v_mov_b32_e32 v133, v0
	v_pk_mul_f32 v[104:105], v[104:105], s[8:9] op_sel_hi:[1,0]
	v_pk_mul_f32 v[100:101], v[100:101], s[8:9] op_sel_hi:[1,0]
	v_cvt_pk_fp8_f32 v133, v104, v105
	v_cvt_pk_fp8_f32 v132, v100, v101
	v_pk_mul_f32 v[102:103], v[102:103], s[8:9] op_sel_hi:[1,0]
	v_pk_mul_f32 v[106:107], v[106:107], s[8:9] op_sel_hi:[1,0]
	v_cvt_pk_fp8_f32 v132, v102, v103 op_sel:[0,0,1]
	v_cvt_pk_fp8_f32 v133, v106, v107 op_sel:[0,0,1]
	global_store_dwordx2 v[148:149], v[132:133], off
	s_waitcnt vmcnt(5)
	v_mov_b32_e32 v134, v0
	v_mov_b32_e32 v135, v0
	v_pk_mul_f32 v[112:113], v[112:113], s[8:9] op_sel_hi:[1,0]
	v_pk_mul_f32 v[108:109], v[108:109], s[8:9] op_sel_hi:[1,0]
	v_cvt_pk_fp8_f32 v135, v112, v113
	v_cvt_pk_fp8_f32 v134, v108, v109
	v_pk_mul_f32 v[110:111], v[110:111], s[8:9] op_sel_hi:[1,0]
	v_pk_mul_f32 v[114:115], v[114:115], s[8:9] op_sel_hi:[1,0]
	v_cvt_pk_fp8_f32 v134, v110, v111 op_sel:[0,0,1]
	v_cvt_pk_fp8_f32 v135, v114, v115 op_sel:[0,0,1]
	v_add_co_u32_e32 v148, vcc, 0x80000, v148
	s_nop 1
	v_addc_co_u32_e32 v149, vcc, 0, v149, vcc
	global_store_dwordx2 v[148:149], v[134:135], off
	s_waitcnt vmcnt(4)
	v_mov_b32_e32 v136, v0
	v_mov_b32_e32 v137, v0
	v_pk_mul_f32 v[120:121], v[120:121], s[8:9] op_sel_hi:[1,0]
	v_pk_mul_f32 v[116:117], v[116:117], s[8:9] op_sel_hi:[1,0]
	v_cvt_pk_fp8_f32 v137, v120, v121
	v_cvt_pk_fp8_f32 v136, v116, v117
	v_pk_mul_f32 v[118:119], v[118:119], s[8:9] op_sel_hi:[1,0]
	v_pk_mul_f32 v[122:123], v[122:123], s[8:9] op_sel_hi:[1,0]
	v_cvt_pk_fp8_f32 v136, v118, v119 op_sel:[0,0,1]
	v_cvt_pk_fp8_f32 v137, v122, v123 op_sel:[0,0,1]
	v_add_co_u32_e32 v148, vcc, 0x80000, v148
	s_nop 1
	v_addc_co_u32_e32 v149, vcc, 0, v149, vcc
	global_store_dwordx2 v[148:149], v[136:137], off
	s_waitcnt vmcnt(3)
	v_mov_b32_e32 v138, v0
	v_mov_b32_e32 v139, v0
	v_pk_mul_f32 v[128:129], v[128:129], s[8:9] op_sel_hi:[1,0]
	v_pk_mul_f32 v[124:125], v[124:125], s[8:9] op_sel_hi:[1,0]
	v_cvt_pk_fp8_f32 v139, v128, v129
	v_cvt_pk_fp8_f32 v138, v124, v125
	v_pk_mul_f32 v[126:127], v[126:127], s[8:9] op_sel_hi:[1,0]
	v_pk_mul_f32 v[130:131], v[130:131], s[8:9] op_sel_hi:[1,0]
	v_cvt_pk_fp8_f32 v138, v126, v127 op_sel:[0,0,1]
	v_cvt_pk_fp8_f32 v139, v130, v131 op_sel:[0,0,1]
	v_add_co_u32_e32 v148, vcc, 0x80000, v148
	s_nop 1
	v_addc_co_u32_e32 v149, vcc, 0, v149, vcc
	global_store_dwordx2 v[148:149], v[138:139], off
	s_branch .LBB0_1291
.Lcv_u_orig:
	v_lshl_add_u64 v[30:31], s[20:21], 0, v[4:5]
	global_load_dwordx4 v[26:29], v[30:31], off offset:16
	s_nop 0
	global_load_dwordx4 v[30:33], v[30:31], off
	v_mov_b32_e32 v34, v0
	v_mov_b32_e32 v35, v0
	s_waitcnt vmcnt(0)
	v_pk_mul_f32 v[26:27], v[26:27], s[8:9] op_sel_hi:[1,0]
	v_pk_mul_f32 v[30:31], v[30:31], s[8:9] op_sel_hi:[1,0]
	v_cvt_pk_fp8_f32 v35, v26, v27
	v_cvt_pk_fp8_f32 v34, v30, v31
	v_pk_mul_f32 v[32:33], v[32:33], s[8:9] op_sel_hi:[1,0]
	v_pk_mul_f32 v[28:29], v[28:29], s[8:9] op_sel_hi:[1,0]
	v_cvt_pk_fp8_f32 v34, v32, v33 op_sel:[0,0,1]
	v_cvt_pk_fp8_f32 v35, v28, v29 op_sel:[0,0,1]
	global_store_dwordx2 v[2:3], v[34:35], off
	s_branch .LBB0_1291
